# baseline (speedup 1.0000x reference)
.LBB2_27:
	v_mov_b32_e32 v58, 1.0

.LBB2_30:
	v_subrev_u32_e32 v50, s92, v184
	s_add_i32 s93, s90, 0
	v_add_u32_e32 v50, s93, v50
	v_subrev_u32_e32 v150, s92, v191
	ds_read_b128 v[192:195], v150 offset:36864
	ds_read_b128 v[50:53], v50
	ds_read_b128 v[196:199], v150 offset:33792
	s_add_i32 s80, s86, s88
	s_waitcnt lgkmcnt(1)
	v_mfma_f32_32x32x16_f16 v[82:97], v[50:53], v[154:157], v[66:81]
	v_add_f32_e32 v54, v114, v115
	ds_read_b128 v[200:203], v150 offset:37888
	v_add_f32_e32 v54, v116, v54
	v_add_f32_e32 v54, v117, v54
	v_add_f32_e32 v54, v118, v54
	v_add_f32_e32 v54, v119, v54
	v_cvt_pk_f16_f32 v166, v114, v115
	v_cvt_pk_f16_f32 v167, v116, v117
	s_nop 0
	v_add_f32_e32 v50, v120, v54
	v_add_f32_e32 v50, v121, v50
	v_add_f32_e32 v50, v122, v50
	v_add_f32_e32 v151, v123, v50
	v_mfma_f32_32x32x16_f16 v[50:65], v[192:195], v[154:157], v[66:81]
	ds_read_b128 v[114:117], v150 offset:34816
	v_cvt_pk_f16_f32 v168, v118, v119
	v_cvt_pk_f16_f32 v169, v120, v121
	s_waitcnt lgkmcnt(2)
	v_mfma_f32_32x32x16_f16 v[82:97], v[196:199], v[146:149], v[82:97]
	ds_read_b128 v[118:121], v150 offset:38912
	v_add_f32_e32 v151, v124, v151
	v_add_f32_e32 v151, v125, v151
	v_add_f32_e32 v151, v126, v151
	v_add_f32_e32 v151, v127, v151
	v_cvt_pk_f16_f32 v162, v122, v123
	v_cvt_pk_f16_f32 v163, v124, v125
	s_waitcnt lgkmcnt(2)
	v_mfma_f32_32x32x16_f16 v[50:65], v[200:203], v[146:149], v[50:65]
	ds_read_b128 v[122:125], v150 offset:35840
	v_add_f32_e32 v151, v128, v151
	v_add_f32_e32 v151, v129, v151
	v_add_f32_e32 v151, v98, v151
	v_add_f32_e32 v151, v99, v151
	v_cvt_pk_f16_f32 v164, v126, v127
	v_cvt_pk_f16_f32 v165, v128, v129
	s_waitcnt lgkmcnt(2)
	v_mfma_f32_32x32x16_f16 v[82:97], v[114:117], v[142:145], v[82:97]
	ds_read_b128 v[126:129], v150 offset:39936
	v_add_f32_e32 v150, v100, v151
	v_add_f32_e32 v150, v101, v150
	v_add_f32_e32 v150, v102, v150
	v_add_f32_e32 v150, v103, v150
	v_cvt_pk_f16_f32 v158, v98, v99
	v_cvt_pk_f16_f32 v159, v100, v101
	s_waitcnt lgkmcnt(2)
	v_mfma_f32_32x32x16_f16 v[50:65], v[118:121], v[142:145], v[50:65]
	ds_read_b128 v[114:117], v190 offset:24576
	v_add_f32_e32 v98, v104, v150
	v_add_f32_e32 v98, v105, v98
	v_add_f32_e32 v98, v106, v98
	v_add_f32_e32 v98, v107, v98
	v_cvt_pk_f16_f32 v160, v102, v103
	v_cvt_pk_f16_f32 v161, v104, v105
	s_waitcnt lgkmcnt(2)
	v_mfma_f32_32x32x16_f16 v[82:97], v[122:125], v[138:141], v[82:97]
	ds_read_b128 v[102:105], v190 offset:25600
	v_add_f32_e32 v98, v108, v98
	v_add_f32_e32 v98, v109, v98
	v_add_f32_e32 v98, v110, v98
	v_add_f32_e32 v118, v111, v98
	v_cvt_pk_f16_f32 v150, v106, v107
	v_cvt_pk_f16_f32 v151, v108, v109
	s_waitcnt lgkmcnt(2)
	v_mfma_f32_32x32x16_f16 v[50:65], v[126:129], v[138:141], v[50:65]
	ds_read_b128 v[98:101], v190 offset:26624
	v_add_f32_e32 v106, v112, v118
	v_add_f32_e32 v106, v113, v106
	v_add_f32_e32 v106, 0, v106
	v_cvt_pk_f16_f32 v152, v110, v111
	v_cvt_pk_f16_f32 v153, v112, v113
	s_cmp_lg_u32 s80, 1
	s_cbranch_scc1 .LBB2_32
	s_or_b64 vcc, s[62:63], s[58:59]
	v_cndmask_b32_e32 v96, v188, v96, vcc
	s_or_b64 vcc, vcc, s[54:55]
	v_cndmask_b32_e32 v95, v188, v95, vcc
	s_or_b64 vcc, vcc, s[50:51]
	v_cndmask_b32_e32 v94, v188, v94, vcc
	s_or_b64 vcc, vcc, s[46:47]
	v_cndmask_b32_e32 v93, v188, v93, vcc
	s_or_b64 vcc, vcc, s[42:43]
	v_cndmask_b32_e32 v92, v188, v92, vcc
	s_or_b64 vcc, vcc, s[38:39]
	v_cndmask_b32_e32 v91, v188, v91, vcc
	s_or_b64 vcc, vcc, s[34:35]
	v_cndmask_b32_e32 v90, v188, v90, vcc
	s_or_b64 vcc, vcc, s[28:29]
	v_cndmask_b32_e32 v89, v188, v89, vcc
	s_or_b64 vcc, vcc, s[24:25]
	v_cndmask_b32_e32 v88, v188, v88, vcc
	s_or_b64 vcc, vcc, s[20:21]
	v_cndmask_b32_e32 v87, v188, v87, vcc
	s_or_b64 vcc, vcc, s[16:17]
	v_cndmask_b32_e32 v86, v188, v86, vcc
	s_or_b64 vcc, vcc, s[12:13]
	v_cndmask_b32_e32 v85, v188, v85, vcc
	s_or_b64 vcc, vcc, s[8:9]
	v_cndmask_b32_e32 v84, v188, v84, vcc
	s_or_b64 vcc, vcc, s[4:5]
	v_cndmask_b32_e32 v83, v188, v83, vcc
	s_or_b64 vcc, vcc, s[0:1]
	v_cndmask_b32_e32 v82, v188, v82, vcc
	s_or_b64 vcc, s[64:65], s[60:61]
	v_cndmask_b32_e32 v64, v188, v64, vcc
	s_or_b64 vcc, vcc, s[56:57]
	v_cndmask_b32_e32 v63, v188, v63, vcc
	s_or_b64 vcc, vcc, s[52:53]
	v_cndmask_b32_e32 v62, v188, v62, vcc
	s_or_b64 vcc, vcc, s[48:49]
	v_cndmask_b32_e32 v61, v188, v61, vcc
	s_or_b64 vcc, vcc, s[44:45]
	v_cndmask_b32_e32 v60, v188, v60, vcc
	s_or_b64 vcc, vcc, s[40:41]
	v_cndmask_b32_e32 v59, v188, v59, vcc
	s_or_b64 vcc, vcc, s[36:37]
	v_cndmask_b32_e32 v58, v188, v58, vcc
	s_or_b64 vcc, vcc, s[30:31]
	v_cndmask_b32_e32 v57, v188, v57, vcc
	s_or_b64 vcc, vcc, s[26:27]
	v_cndmask_b32_e32 v56, v188, v56, vcc
	s_or_b64 vcc, vcc, s[22:23]
	v_cndmask_b32_e32 v55, v188, v55, vcc
	s_or_b64 vcc, vcc, s[18:19]
	v_cndmask_b32_e32 v54, v188, v54, vcc
	s_or_b64 vcc, vcc, s[14:15]
	v_cndmask_b32_e32 v53, v188, v53, vcc
	s_or_b64 vcc, vcc, s[10:11]
	v_cndmask_b32_e32 v52, v188, v52, vcc
	s_or_b64 vcc, vcc, s[6:7]
	v_cndmask_b32_e32 v51, v188, v51, vcc
	s_or_b64 vcc, vcc, s[2:3]
	v_cndmask_b32_e64 v97, v188, v97, s[62:63]
	v_cndmask_b32_e64 v65, v188, v65, s[64:65]
	v_cndmask_b32_e32 v50, v188, v50, vcc

.LBB2_37:
	v_mov_b32_e32 v17, 0
	v_mov_b32_e32 v16, v17
	v_mov_b32_e32 v15, v17
	v_mov_b32_e32 v14, v17
	v_mov_b32_e32 v13, v17
	v_mov_b32_e32 v12, v17
	v_mov_b32_e32 v11, v17
	v_mov_b32_e32 v10, v17
	v_mov_b32_e32 v9, v17
	v_mov_b32_e32 v8, v17
	v_mov_b32_e32 v7, v17
	v_mov_b32_e32 v6, v17
	v_mov_b32_e32 v5, v17
	v_mov_b32_e32 v4, v17
	v_mov_b32_e32 v3, v17
	v_mov_b32_e32 v2, v17
	v_mov_b32_e32 v33, v17
	v_mov_b32_e32 v32, v17
	v_mov_b32_e32 v31, v17
	v_mov_b32_e32 v30, v17
	v_mov_b32_e32 v29, v17
	v_mov_b32_e32 v28, v17
	v_mov_b32_e32 v27, v17
	v_mov_b32_e32 v26, v17
	v_mov_b32_e32 v25, v17
	v_mov_b32_e32 v24, v17
	v_mov_b32_e32 v23, v17
	v_mov_b32_e32 v22, v17
	v_mov_b32_e32 v21, v17
	v_mov_b32_e32 v20, v17
	v_mov_b32_e32 v19, v17
	v_mov_b32_e32 v18, v17
	v_mov_b32_e32 v189, v17
	s_branch .LBB2_38
.Lat_exit:
	v_mov_b64_e32 v[34:35], v[66:67]
	v_mov_b64_e32 v[36:37], v[68:69]
	v_mov_b64_e32 v[38:39], v[70:71]
	v_mov_b64_e32 v[40:41], v[72:73]
	v_mov_b64_e32 v[42:43], v[74:75]
	v_mov_b64_e32 v[44:45], v[76:77]
	v_mov_b64_e32 v[46:47], v[78:79]
	v_mov_b64_e32 v[48:49], v[80:81]
